# softmax scale folded into the q gain of the layer-1 QK-norm phase (when the fixed-reference body runs) and QK accumulators started at -m*C: no per-score fma in the diff16 tile loop
# speedup vs baseline: 1.0099x; 1.0034x over previous
; template <int NQ, int NK, bool CTXQ, bool GATES>
; __device__ __forceinline__ void phase_qknorm(const Args& a, int lane, int wave, int bid, int G, int ld, int qcol0, int kcol0, const float* qg, const float* kg) {
;     unsigned char* ws = a.ws; bf16* P = (bf16*)(ws + WS_PROJ); const float* TAB = (const float*)(ws + WS_TAB);
;     const int gw = bid * NWAVES + wave, NGW = G * NWAVES;
;     if (GATES) {
;         const float* Gt = (const float*)(ws + WS_G); float* GP = (float*)(ws + WS_GP); float* GSC = (float*)(ws + WS_GS) + 8 * NCH * 4;
;         for (int it = gw; it < 8 * NCH; it += NGW) {
;             const int dh = it / NCH, c = it % NCH, dir = dh >> 2, head = dh & 3;
;             const int row = seq_row(dir, c, lane);
;             const float gi = Gt[(size_t)row * 16 + dir * 8 + head], gf = Gt[(size_t)row * 16 + dir * 8 + 4 + head];
;             const float fc = fminf(gf, 0.f) - log1pf(expf(-fabsf(gf)));
;             float bc = fc;
; #pragma unroll
;             for (int o = 1; o < 64; o <<= 1) { const float t = __shfl_up(bc, o); if (lane >= o) bc += t; }
;             const float av = gi - bc; float pm = av;
; #pragma unroll
;             for (int o = 1; o < 64; o <<= 1) { const float t = __shfl_up(pm, o); if (lane >= o) pm = fmaxf(pm, t); }
;             float* gp = GP + (size_t)it * 192; gp[lane] = av; gp[64 + lane] = pm; gp[128 + lane] = bc;
;             const float blast = __shfl(bc, 63), pml = __shfl(pm, 63);
;             if (lane == 0) { GSC[it * 2] = blast; GSC[it * 2 + 1] = blast + pml; }
;         }
;     }
;     const float q0 = qg[2 * lane], q1 = qg[2 * lane + 1], k0 = kg[2 * lane], k1 = kg[2 * lane + 1];
;     for (int t = gw; t < NTOK; t += NGW) {
;         const bool lat = t < SEQ; unsigned* base = (unsigned*)(P + (size_t)t * ld) + lane;
;         float c = 1.f, s = 0.f;
;         if (lat) { const int pos = lane < 32 ? (t >> 6) : (t & 63); const float* tp = TAB + 2 * (pos * 32 + (lane & 31)); c = tp[0]; s = tp[1]; }
;         const bool doq = lat || CTXQ;
;         unsigned uq[NQ], uk[NK];
;         if (doq) {
; #pragma unroll
;             for (int i = 0; i < NQ; ++i) uq[i] = base[(qcol0 + i * 128) >> 1]; }
; #pragma unroll
;         for (int i = 0; i < NK; ++i) uk[i] = base[(kcol0 + i * 128) >> 1];
.LBB0_1173:
	s_cmp_lt_i32 s80, 15
	s_cselect_b64 s[0:1], -1, 0
	s_and_b64 s[8:9], s[0:1], s[6:7]
	s_andn2_b64 vcc, exec, s[8:9]
	s_cbranch_vccnz .LBB0_1185
	v_readfirstlane_b32 s0, v0
	s_lshr_b32 s2, s0, 6
	s_lshl_b32 s3, s94, 3
	s_add_i32 s0, s2, s3
	s_mov_b64 s[4:5], s[96:97]
	s_cmpk_gt_i32 s0, 0x40ff
	s_cbranch_scc1 .LBB0_1185
	s_load_dwordx2 s[6:7], s[4:5], 0xe8
	s_load_dword s16, s[96:97], 0xf8
	s_load_dwordx4 s[12:15], s[4:5], 0x80
	v_and_b32_e32 v2, 63, v0
	v_lshlrev_b32_e32 v4, 3, v2
	v_lshlrev_b32_e32 v3, 1, v0
	v_and_b32_e32 v58, 62, v3
	s_waitcnt lgkmcnt(0)
	global_load_dwordx2 v[18:19], v4, s[12:13]
	global_load_dwordx2 v[20:21], v4, s[14:15]
	v_mbcnt_lo_u32_b32 v3, -1, 0
	v_mbcnt_hi_u32_b32 v3, -1, v3
	v_and_b32_e32 v4, 64, v3
	v_add_u32_e32 v4, 64, v4
	v_xor_b32_e32 v5, 1, v3
	v_cmp_lt_i32_e32 vcc, v5, v4
	s_add_u32 s10, s6, 0x100000
	s_addc_u32 s11, s7, 0
	v_cndmask_b32_e32 v5, v3, v5, vcc
	v_lshlrev_b32_e32 v59, 2, v5
	v_xor_b32_e32 v5, 2, v3
	v_cmp_lt_i32_e32 vcc, v5, v4
	s_lshl_b32 s1, s16, 3
	s_ashr_i32 s12, s3, 31
	v_cndmask_b32_e32 v5, v3, v5, vcc
	v_lshlrev_b32_e32 v60, 2, v5
	v_xor_b32_e32 v5, 4, v3
	v_cmp_lt_i32_e32 vcc, v5, v4
	s_add_u32 s2, s2, s3
	s_addc_u32 s3, 0, s12
	v_cndmask_b32_e32 v5, v3, v5, vcc
	v_lshlrev_b32_e32 v61, 2, v5
	v_xor_b32_e32 v5, 8, v3
	v_cmp_lt_i32_e32 vcc, v5, v4
	s_mulk_i32 s3, 0x3000
	s_mul_hi_u32 s12, s2, 0x3000
	v_cndmask_b32_e32 v5, v3, v5, vcc
	v_lshlrev_b32_e32 v62, 2, v5
	v_xor_b32_e32 v5, 16, v3
	v_cmp_lt_i32_e32 vcc, v5, v4
	s_add_i32 s12, s12, s3
	s_mulk_i32 s2, 0x3000
	v_cndmask_b32_e32 v5, v3, v5, vcc
	v_lshlrev_b32_e32 v63, 2, v5
	v_xor_b32_e32 v5, 32, v3
	v_cmp_lt_i32_e32 vcc, v5, v4
	s_add_u32 s2, s6, s2
	v_lshlrev_b32_e32 v16, 2, v2
	v_cndmask_b32_e32 v3, v3, v5, vcc
	v_mov_b32_e32 v17, 0
	s_addc_u32 s3, s7, s12
	v_cmp_gt_u32_e64 s[4:5], 32, v2
	v_lshlrev_b32_e32 v64, 2, v3
	v_lshl_add_u64 v[2:3], s[2:3], 0, v[16:17]
	s_mov_b64 s[2:3], 0x36552400
	v_lshl_add_u64 v[22:23], v[2:3], 0, s[2:3]
	s_mul_i32 s12, s16, 0x18000
	s_mul_hi_i32 s13, s1, 0x3000
	v_mov_b32_e32 v2, v17
	v_mov_b32_e32 v4, v17
	v_mov_b32_e32 v3, v17
	v_mov_b32_e32 v6, v17
	v_mov_b32_e32 v5, v17
	v_mov_b32_e32 v8, v17
	v_mov_b32_e32 v7, v17
	v_mov_b32_e32 v10, v17
	v_mov_b32_e32 v9, v17
	v_mov_b32_e32 v12, v17
	v_mov_b32_e32 v11, v17
	v_mov_b32_e32 v14, v17
	v_mov_b32_e32 v13, v17
	v_mov_b32_e32 v16, v17
	s_mov_b64 s[14:15], 0x1000
	s_mov_b64 s[16:17], 0x1100
	s_mov_b64 s[18:19], 0x1200
	s_mov_b64 s[20:21], 0x1300
	s_mov_b64 s[22:23], 0x1400
	s_mov_b64 s[24:25], 0x1500
	s_mov_b64 s[26:27], 0x1600
	s_mov_b64 s[28:29], 0x1700
	s_mov_b64 s[30:31], 0x1800
	s_mov_b64 s[34:35], 0x1900
	s_mov_b64 s[36:37], 0x1a00
	s_mov_b64 s[38:39], 0x1b00
	s_mov_b64 s[40:41], 0x1c00
	s_mov_b64 s[42:43], 0x1d00
	s_mov_b64 s[44:45], 0x1e00
	s_mov_b64 s[46:47], 0x1f00
	v_mov_b32_e32 v65, 0x358637bd
	s_mov_b32 s2, 0xf800000
	s_waitcnt vmcnt(0)
	v_mov_b32_e32 v66, 0x260
	v_mov_b32_e32 v15, v17
	v_max_f32_e64 v96, |v18|, |v19|
	v_max_f32_e64 v97, |v20|, |v21|
	ds_bpermute_b32 v98, v59, v96
	ds_bpermute_b32 v99, v59, v97
	s_waitcnt lgkmcnt(0)
	v_max_f32_e32 v96, v96, v98
	v_max_f32_e32 v97, v97, v99
	ds_bpermute_b32 v98, v60, v96
	ds_bpermute_b32 v99, v60, v97
	s_waitcnt lgkmcnt(0)
	v_max_f32_e32 v96, v96, v98
	v_max_f32_e32 v97, v97, v99
	ds_bpermute_b32 v98, v61, v96
	ds_bpermute_b32 v99, v61, v97
	s_waitcnt lgkmcnt(0)
	v_max_f32_e32 v96, v96, v98
	v_max_f32_e32 v97, v97, v99
	ds_bpermute_b32 v98, v62, v96
	ds_bpermute_b32 v99, v62, v97
	s_waitcnt lgkmcnt(0)
	v_max_f32_e32 v96, v96, v98
	v_max_f32_e32 v97, v97, v99
	ds_bpermute_b32 v98, v63, v96
	ds_bpermute_b32 v99, v63, v97
	s_waitcnt lgkmcnt(0)
	v_max_f32_e32 v96, v96, v98
	v_max_f32_e32 v97, v97, v99
	ds_bpermute_b32 v98, v64, v96
	ds_bpermute_b32 v99, v64, v97
	s_waitcnt lgkmcnt(0)
	v_max_f32_e32 v96, v96, v98
	v_max_f32_e32 v97, v97, v99
	v_mul_f32_e32 v96, 0x43000000, v96
	v_mul_f32_e32 v96, v96, v97
	v_add_f32_e32 v96, v96, v96
	v_mul_f32_e32 v96, 0x3db504f3, v96
	v_mov_b32_e32 v98, 0x3e0293ee
	v_mov_b32_e32 v99, 1.0
	v_cmp_gt_f32_e32 vcc, 0x42a00000, v96
	v_cndmask_b32_e32 v98, v99, v98, vcc
	v_mul_f32_e32 v18, v18, v98
	v_mul_f32_e32 v19, v19, v98
	s_branch .LBB0_1177

; template <int LDQ, int LDK, int LDV, int LDO, int DMX> ...
;   const int tid = threadIdx.x, wid = tid >> 6, lane = tid & 63, l16 = lane & 15, g = lane >> 4, rb = wid & 3, ch = wid >> 2;
;   char* V_lds = lds; char* K_lds = lds + D16_OFF_K; float* L_lds = (float*)(lds + D16_OFF_L); float* S_lds = L_lds + 8 * 32;
;   char* P_own = lds + D16_OFF_P + rb * PB_P + ch * 2048 + lane * 16; char* P_oth = lds + D16_OFF_P + rb * PB_P + (1 - ch) * 2048 + lane * 16;
;   constexpr float C = SCALE * 1.4426950408889634f; const float mnC = -mref * C;
;   const int sr = tid >> 4, sc = (tid & 15) * 8;
;   const int vst0 = (sc >> 4) * VP16 + sr * 32 + ((sc >> 3) & 1) * 16, vst1 = vst0 + 1024;
;   const int vlane = (int)(uintptr_t)V_lds + ch * (8 * VP16) + (4 * g + (l16 >> 2)) * 32 + (l16 & 3) * 8;
;   const int kb0 = (32 * ch + l16) * 272 + g * 16;
;   bf16x8 sv0, sv1, sv2, sv3, sk0, sk1;
;   const unsigned koff0 = (unsigned)(sr * LDK + sc) * 2u, koff1 = koff0 + 32u * LDK * 2u, voff0 = (unsigned)(sr * LDV + sc) * 2u, voff1 = voff0 + 32u * LDV * 2u;
; __global__ void __launch_bounds__(NWAVES * 64, 2) __attribute__((amdgpu_num_vgpr(248))) mega_fwd(Args args) {
;     ...
;             const float lam_init = 0.8f - 0.6f * expf(-0.3f);
;             const float d1 = wave_sum(la.in[I_LQ1][lane] * la.in[I_LK1][lane] + la.in[I_LQ1][64 + lane] * la.in[I_LK1][64 + lane]);
;             const float d2 = wave_sum(la.in[I_LQ2][lane] * la.in[I_LK2][lane] + la.in[I_LQ2][64 + lane] * la.in[I_LK2][64 + lane]);
;             const float lam = expf(d1) - expf(d2) + lam_init;
.LBB0_1261:
	s_andn2_saveexec_b64 s[8:9], s[30:31]
	s_cbranch_execz .LBB0_1283
	s_load_dwordx8 s[12:19], s[28:29], 0x90
	s_cmpk_gt_i32 s94, 0x3ff
	s_waitcnt lgkmcnt(0)
	global_load_dword v12, v6, s[12:13]
	global_load_dword v13, v6, s[14:15]
	global_load_dword v14, v6, s[12:13] offset:256
	global_load_dword v15, v6, s[14:15] offset:256
	global_load_dword v16, v6, s[16:17] offset:256
	global_load_dword v17, v6, s[18:19] offset:256
	global_load_dword v18, v6, s[16:17]
	global_load_dword v19, v6, s[18:19]
	s_waitcnt vmcnt(0)
	v_mul_f32_e32 v6, v14, v15
	v_fmac_f32_e32 v6, v12, v13
	v_mul_f32_e32 v14, v16, v17
	ds_bpermute_b32 v12, v8, v6
	v_fmac_f32_e32 v14, v18, v19
	ds_bpermute_b32 v8, v8, v14
	s_waitcnt lgkmcnt(1)
	v_add_f32_e32 v6, v6, v12
	ds_bpermute_b32 v12, v9, v6
	s_waitcnt lgkmcnt(1)
	v_add_f32_e32 v8, v14, v8
	ds_bpermute_b32 v9, v9, v8
	s_waitcnt lgkmcnt(1)
	v_add_f32_e32 v6, v6, v12
	s_waitcnt lgkmcnt(0)
	v_add_f32_e32 v8, v8, v9
	ds_bpermute_b32 v9, v10, v6
	ds_bpermute_b32 v10, v10, v8
	s_waitcnt lgkmcnt(1)
	v_add_f32_e32 v6, v6, v9
	s_waitcnt lgkmcnt(0)
	v_add_f32_e32 v8, v8, v10
	ds_bpermute_b32 v9, v11, v6
	ds_bpermute_b32 v10, v11, v8
	s_waitcnt lgkmcnt(1)
	v_add_f32_e32 v6, v6, v9
	s_waitcnt lgkmcnt(0)
	v_add_f32_e32 v8, v8, v10
	ds_bpermute_b32 v9, v185, v6
	ds_bpermute_b32 v10, v185, v8
	s_waitcnt lgkmcnt(1)
	v_add_f32_e32 v9, v6, v9
	s_waitcnt lgkmcnt(0)
	v_add_f32_e32 v6, v8, v10
	ds_bpermute_b32 v10, v186, v9
	ds_bpermute_b32 v8, v186, v6
	s_cbranch_scc1 .LBB0_1283
	v_lshlrev_b32_e32 v12, 6, v0
	v_lshrrev_b32_e32 v11, 8, v0
	v_and_b32_e32 v12, 0x3000, v12
	s_add_i32 s4, 0, 0x18c00
	v_lshrrev_b32_e32 v189, 4, v2
	v_add_u32_e32 v12, s4, v12
	v_lshlrev_b32_e32 v13, 11, v11
	v_lshlrev_b32_e32 v2, 4, v2
	v_add3_u32 v190, v12, v13, v2
	v_xor_b32_e32 v13, 1, v11
	v_lshlrev_b32_e32 v14, 11, v13
	v_add3_u32 v191, v12, v14, v2
	v_lshrrev_b32_e32 v2, 4, v3
	v_lshlrev_b32_e32 v1, 5, v1
	s_movk_i32 s4, 0x820
	v_and_b32_e32 v188, 15, v0
	v_mad_u32_u24 v1, v2, s4, v1
	s_add_i32 s4, 0, 0x10400
	v_and_or_b32 v1, v5, 16, v1
	v_lshl_or_b32 v5, v11, 5, v188
	s_cmp_lg_u32 0, -1
	v_mul_u32_u24_e32 v5, 0x110, v5
	v_and_b32_e32 v12, 48, v0
	s_cselect_b32 s5, 0, 0
	v_add3_u32 v193, s4, v5, v12
	s_movk_i32 s6, 0x4100
	v_mov_b32_e32 v5, s5
	v_lshlrev_b32_e32 v2, 7, v189
	v_mad_u32_u24 v5, v11, s6, v5
	v_add3_u32 v194, v5, v3, v2
	s_waitcnt lgkmcnt(1)
	v_add_f32_e32 v3, v9, v10
	s_mov_b32 s6, 0x3fb8aa3b
	v_mul_f32_e32 v5, 0x3fb8aa3b, v3
	v_fma_f32 v9, v3, s6, -v5
	v_rndne_f32_e32 v10, v5
	v_fmac_f32_e32 v9, 0x32a5705f, v3
	v_sub_f32_e32 v5, v5, v10
	v_add_f32_e32 v5, v5, v9
	v_exp_f32_e32 v5, v5
	v_cvt_i32_f32_e32 v9, v10
	v_lshlrev_b32_e32 v195, 10, v11
	v_lshlrev_b32_e32 v196, 10, v13
	v_add_u32_e32 v2, 0x8200, v194
	v_add_u32_e32 v197, v2, v195
	v_add_u32_e32 v199, v2, v196
	v_ldexp_f32 v2, v5, v9
	s_waitcnt lgkmcnt(0)
	v_add_f32_e32 v5, v6, v8
	v_mul_f32_e32 v6, 0x3fb8aa3b, v5
	v_fma_f32 v8, v5, s6, -v6
	v_rndne_f32_e32 v9, v6
	v_fmac_f32_e32 v8, 0x32a5705f, v5
	v_sub_f32_e32 v6, v6, v9
	v_add_f32_e32 v6, v6, v8
	v_exp_f32_e32 v6, v6
	v_cvt_i32_f32_e32 v8, v9
	s_mov_b32 s7, 0xc2ce8ed0
	v_cmp_ngt_f32_e32 vcc, s7, v3
	s_mov_b32 s12, 0x42b17218
	v_mov_b32_e32 v9, 0x7f800000
	v_cndmask_b32_e32 v2, 0, v2, vcc
	v_cmp_nlt_f32_e32 vcc, s12, v3
	s_add_u32 s30, s26, 0x42852400
	v_ldexp_f32 v3, v6, v8
	v_cndmask_b32_e32 v2, v9, v2, vcc
	v_cmp_ngt_f32_e32 vcc, s7, v5
	s_load_dwordx2 s[10:11], s[28:29], 0xb0
	s_addc_u32 s31, s27, 0
	v_cndmask_b32_e32 v3, 0, v3, vcc
	v_cmp_nlt_f32_e32 vcc, s12, v5
	s_add_u32 s34, s26, 0x36553400
	v_mov_b32_e32 v159, 0
	v_cndmask_b32_e32 v3, v9, v3, vcc
	v_sub_f32_e32 v2, v2, v3
	s_addc_u32 s35, s27, 0
	v_lshlrev_b32_e32 v4, 1, v4
	v_add_u32_e32 v198, s4, v184
	s_movk_i32 s4, 0xff
	v_add_f32_e32 v160, 0x3eb60549, v2
	s_add_u32 s36, s26, 0x36554400
	v_lshl_add_u32 v4, v188, 4, v4
	v_mov_b32_e32 v5, v159
	v_lshrrev_b32_e32 v187, 6, v0
	s_movk_i32 s28, 0x3000
	v_add_u32_e32 v1, 0, v1
	s_mov_b32 s29, 0x60000
	v_add_u32_e32 v158, 0x60000, v156
	v_cmp_lt_u32_e64 s[4:5], s4, v0
	s_addc_u32 s37, s27, 0
	v_mul_f32_e32 v200, 0xbe0293ee, v7
	v_mov_b32_e32 v248, v200
	v_mov_b32_e32 v249, v200
	v_mov_b32_e32 v250, v200
	v_mov_b32_e32 v251, v200
	v_mov_b32_e32 v161, v160
	v_mov_b32_e32 v2, v160
	v_mov_b32_e32 v3, v160
	v_and_b32_e32 v253, 63, v0
	v_lshrrev_b32_e32 v252, 1, v253
	v_mul_u32_u24_e32 v252, 0x3000, v252
	v_and_b32_e32 v253, 1, v253
	v_lshl_add_u32 v252, v253, 4, v252
	v_lshrrev_b32_e32 v253, 6, v0
	v_lshl_add_u32 v253, v253, 6, v252
	v_lshrrev_b32_e32 v252, 6, v0
	v_mul_u32_u24_e32 v252, 0x1040, v252
	s_nop 0
	v_readfirstlane_b32 s84, v252
	v_lshl_add_u64 v[162:163], s[26:27], 0, v[4:5]
	s_mov_b32 s26, 0x30000
	s_mov_b32 s27, 0xc0000
	s_mov_b32 s38, 0x120000
	s_mov_b32 s39, 0x180000
	s_mov_b32 s40, 0x1e0000
	s_mov_b32 s41, 0x36793000
	s_mov_b32 s42, 0x367f3000
	s_mov_b32 s43, 0x366d4000
	s_mov_b32 s44, 0x36734000
	s_add_i32 s45, 0, 0x20c00
	s_mov_b64 s[12:13], 0x40000
	s_add_i32 s46, 0, 0x21000
	v_mov_b32_e32 v201, 0x358637bd
	s_mov_b32 s47, 0xf800000
	v_mov_b32_e32 v202, 0x260
	s_mov_b32 s48, 0x3f24fd5c
	s_movk_i32 s49, 0x7fff
	s_mov_b64 s[14:15], 0x10000
	v_mov_b32_e32 v203, 1
	s_mov_b32 s50, s94
	s_branch .LBB0_1265

; #define ELOADV(kt) do { const char* vb_ = (const char*)Vh + (size_t)(kt) * (64 * LDV * 2); sv0 = *(const bf16x8*)(vb_ + voff0); sv1 = *(const bf16x8*)(vb_ + voff1); sv2 = *(const bf16x8*)(vb_ + voff0 + 256); sv3 = *(const bf16x8*)(vb_ + voff1 + 256); } while (0)
; #define ELOADK(kt) do { const char* kb_ = (const char*)Kh + (size_t)(kt) * (64 * LDK * 2); sk0 = *(const bf16x8*)(kb_ + koff0); sk1 = *(const bf16x8*)(kb_ + koff1); } while (0)
; #define EWRITEV(b) do { char* d_ = V_lds + (b) * D16_V; *(bf16x8*)(d_ + vst0) = sv0; *(bf16x8*)(d_ + vst1) = sv1; *(bf16x8*)(d_ + 8 * VP16 + vst0) = sv2; *(bf16x8*)(d_ + 8 * VP16 + vst1) = sv3; } while (0)
; #define EWRITEK(b) do { char* d_ = K_lds + (b) * PB_K; *(bf16x8*)(d_ + KSWZ(sr, sc * 2)) = sk0; *(bf16x8*)(d_ + KSWZ(32 + sr, sc * 2)) = sk1; } while (0)
; template <int LDQ, int LDK, int LDV, int LDO, int DMX> ...
;     ...
;   { int l16q = l16, gq = g, widq = wid; asm volatile("" : "+v"(l16q), "+v"(gq), "+v"(widq));
;     const bf16* Qw = Qb0 + pass * 128 + (long)((widq & 3) * QBLK + l16q) * LDQ + gq * 8;
; #pragma unroll
;     for (int qt = 0; qt < 2; ++qt)
; #pragma unroll
;       for (int ds = 0; ds < 4; ++ds) qr[qt][ds] = *reinterpret_cast<const bf16x8*>(Qw + (long)qt * 16 * LDQ + ds * 32); }
;   ELOADK(0); ELOADV(0); asm volatile("s_waitcnt vmcnt(0)" ::: "memory"); EWRITEK(0); EWRITEV(0);
;   ELOADK(1); asm volatile("s_waitcnt vmcnt(0)" ::: "memory"); EWRITEK(1); __syncthreads();
;   ELOADK(2); ELOADV(1);
;   EQK(0); ESM(0);
;   if (wid >= 4) __builtin_amdgcn_s_setprio(1);
.LBB0_1267:
	v_mov_b32_e32 v6, v189
	v_mov_b32_e32 v4, v188
	v_mov_b32_e32 v5, v187
	s_lshl_b64 s[22:23], s[6:7], 1
	s_add_u32 s56, s51, s22
	v_lshlrev_b32_e32 v5, 5, v5
	s_addc_u32 s57, s52, s23
	v_and_b32_e32 v5, 0x60, v5
	v_add_u32_e32 v7, v5, v4
	v_mov_b64_e32 v[4:5], s[56:57]
	v_lshlrev_b32_e32 v6, 3, v6
	v_mad_i64_i32 v[4:5], s[56:57], v7, s28, v[4:5]
	v_ashrrev_i32_e32 v7, 31, v6
	v_lshl_add_u64 v[20:21], v[6:7], 1, v[4:5]
	s_add_u32 s22, s53, s22
	v_add_co_u32_e32 v32, vcc, s26, v20
	s_addc_u32 s23, s54, s23
	s_nop 0
	v_addc_co_u32_e32 v33, vcc, 0, v21, vcc
	v_lshl_add_u64 v[76:77], s[22:23], 0, v[156:157]
	v_add_co_u32_e32 v40, vcc, s29, v76
	global_load_dwordx4 v[4:7], v[20:21], off
	global_load_dwordx4 v[8:11], v[20:21], off offset:64
	global_load_dwordx4 v[12:15], v[20:21], off offset:128
	global_load_dwordx4 v[16:19], v[20:21], off offset:192
	v_addc_co_u32_e32 v41, vcc, 0, v77, vcc
	v_add_co_u32_e32 v60, vcc, s27, v76
	global_load_dwordx4 v[20:23], v[32:33], off
	global_load_dwordx4 v[24:27], v[32:33], off offset:64
	global_load_dwordx4 v[28:31], v[32:33], off offset:128
	s_nop 0
	global_load_dwordx4 v[32:35], v[32:33], off offset:192
	v_addc_co_u32_e32 v61, vcc, 0, v77, vcc
	v_add_co_u32_e32 v64, vcc, s38, v76
	global_load_dwordx4 v[36:39], v[76:77], off
	s_nop 0
	global_load_dwordx4 v[40:43], v[40:41], off
	s_nop 0
	global_load_dwordx4 v[44:47], v[164:165], off
	global_load_dwordx4 v[48:51], v[164:165], off offset:256
	global_load_dwordx4 v[52:55], v[166:167], off
	global_load_dwordx4 v[56:59], v[166:167], off offset:256
	s_waitcnt vmcnt(0)
	v_addc_co_u32_e32 v65, vcc, 0, v77, vcc
	global_load_dwordx4 v[60:63], v[60:61], off
	s_nop 0
	global_load_dwordx4 v[64:67], v[64:65], off
	v_add_u32_e32 v68, 0, v184
	v_add_u32_e32 v69, 0x10400, v68
	v_add_u32_e32 v68, 0x14800, v68
	s_waitcnt vmcnt(0)
	ds_write_b128 v69, v[36:39]
	s_waitcnt vmcnt(6)
	ds_write_b128 v69, v[40:43] offset:8704
	s_waitcnt vmcnt(5)
	ds_write_b128 v1, v[44:47]
	s_waitcnt vmcnt(3)
	ds_write_b128 v1, v[52:55] offset:1024
	ds_write_b128 v1, v[48:51] offset:16640
	s_waitcnt vmcnt(2)
	ds_write_b128 v1, v[56:59] offset:17664
	s_waitcnt vmcnt(0)
	s_waitcnt vmcnt(1)
	ds_write_b128 v68, v[60:63]
	s_waitcnt vmcnt(0)
	ds_write_b128 v68, v[64:67] offset:8704
	s_waitcnt lgkmcnt(0)
	s_barrier
	ds_read_b128 v[36:39], v193
	ds_read_b128 v[40:43], v193 offset:64
	ds_read_b128 v[48:51], v193 offset:4352
	ds_read_b128 v[52:55], v193 offset:4416
	s_waitcnt lgkmcnt(3)
	v_mfma_f32_16x16x32_bf16 v[44:47], v[36:39], v[4:7], 0
	v_mfma_f32_16x16x32_bf16 v[36:39], v[36:39], v[20:23], 0
	s_waitcnt lgkmcnt(1)
	v_mfma_f32_16x16x32_bf16 v[56:59], v[48:51], v[4:7], 0
	v_mfma_f32_16x16x32_bf16 v[48:51], v[48:51], v[20:23], 0
	v_mfma_f32_16x16x32_bf16 v[44:47], v[40:43], v[8:11], v[44:47]
	v_mfma_f32_16x16x32_bf16 v[36:39], v[40:43], v[24:27], v[36:39]
	s_waitcnt lgkmcnt(0)
	v_mfma_f32_16x16x32_bf16 v[40:43], v[52:55], v[8:11], v[56:59]
	v_mfma_f32_16x16x32_bf16 v[48:51], v[52:55], v[24:27], v[48:51]
	ds_read_b128 v[52:55], v193 offset:128
	s_nop 0
	ds_read_b128 v[56:59], v193 offset:192
	s_waitcnt lgkmcnt(1)
	v_mfma_f32_16x16x32_bf16 v[44:47], v[52:55], v[12:15], v[44:47]
	v_mfma_f32_16x16x32_bf16 v[36:39], v[52:55], v[28:31], v[36:39]
	ds_read_b128 v[52:55], v193 offset:4480
	ds_read_b128 v[60:63], v193 offset:4544
	s_waitcnt lgkmcnt(1)
	v_mfma_f32_16x16x32_bf16 v[64:67], v[52:55], v[12:15], v[40:43]
	s_nop 2
	v_add_co_u32_e32 v40, vcc, s39, v76
	v_mfma_f32_16x16x32_bf16 v[68:71], v[52:55], v[28:31], v[48:51]
	s_nop 0
	v_addc_co_u32_e32 v41, vcc, 0, v77, vcc
	v_add_co_u32_e32 v42, vcc, s40, v76
	v_mfma_f32_16x16x32_bf16 v[72:75], v[56:59], v[16:19], v[44:47]
	s_nop 0
	v_addc_co_u32_e32 v43, vcc, 0, v77, vcc
	v_mfma_f32_16x16x32_bf16 v[76:79], v[56:59], v[32:35], v[36:39]
	global_load_dwordx4 v[52:55], v[40:41], off
	global_load_dwordx4 v[56:59], v[42:43], off
	s_nop 0
	s_waitcnt lgkmcnt(0)
	v_mfma_f32_16x16x32_bf16 v[64:67], v[60:63], v[16:19], v[64:67]
	v_mfma_f32_16x16x32_bf16 v[68:71], v[60:63], v[32:35], v[68:71]
	v_add_f32_e32 v61, v200, v73
	v_exp_f32_e32 v62, v61
	v_add_f32_e32 v61, v200, v74
	v_add_f32_e32 v60, v200, v72
	v_exp_f32_e32 v72, v61
	v_add_f32_e32 v61, v200, v75
	s_nop 0
	v_add_f32_e32 v64, v200, v64
	v_exp_f32_e32 v74, v61
	v_add_f32_e32 v61, v200, v76
	v_exp_f32_e32 v76, v64
	v_add_f32_e32 v64, v200, v65
	v_add_f32_e32 v73, v200, v78
	v_exp_f32_e32 v78, v64
	v_add_f32_e32 v64, v200, v66
	v_exp_f32_e32 v80, v64
	v_add_f32_e32 v64, v200, v67
	v_exp_f32_e32 v82, v64
	v_add_f32_e32 v64, v200, v68
	v_add_f32_e32 v63, v200, v77
	v_exp_f32_e32 v77, v64
	v_add_f32_e32 v64, v200, v69
	v_add_f32_e32 v75, v200, v79
	v_exp_f32_e32 v79, v64
	v_add_f32_e32 v64, v200, v70
	v_exp_f32_e32 v81, v64
	v_add_f32_e32 v64, v200, v71
	v_exp_f32_e32 v60, v60
	v_exp_f32_e32 v61, v61
	v_exp_f32_e32 v63, v63
	v_exp_f32_e32 v73, v73
	v_exp_f32_e32 v75, v75
	v_exp_f32_e32 v83, v64
	v_cvt_pk_bf16_f32 v64, v60, v62
	v_cvt_pk_bf16_f32 v65, v72, v74
	v_cvt_pk_bf16_f32 v66, v76, v78
	v_cvt_pk_bf16_f32 v67, v80, v82
	v_cvt_pk_bf16_f32 v68, v61, v63
	v_cvt_pk_bf16_f32 v69, v73, v75
	v_cvt_pk_bf16_f32 v70, v77, v79
	v_cvt_pk_bf16_f32 v71, v81, v83
	ds_write_b128 v190, v[64:67]
	ds_write_b128 v190, v[68:71] offset:1024
	s_and_saveexec_b64 s[22:23], s[4:5]
	s_setprio 1
	s_or_b64 exec, exec, s[22:23]
	v_pk_add_f32 v[60:61], v[60:61], v[62:63]
	v_pk_add_f32 v[62:63], v[72:73], v[74:75]
	v_pk_add_f32 v[72:73], v[80:81], v[82:83]
	v_pk_add_f32 v[60:61], v[60:61], v[62:63]
	v_pk_add_f32 v[62:63], v[76:77], v[78:79]
	v_mov_b32_e32 v112, 0
	v_pk_add_f32 v[62:63], v[62:63], v[72:73]
	s_xor_b64 s[20:21], s[20:21], -1
; #define SBAR() __builtin_amdgcn_sched_barrier(0)
; template <int LDQ, int LDK, int LDV, int LDO, int DMX> ...
;     ...
;   for (int t = 0; t < NT; ++t) {
;     __syncthreads();
;     bf16x8 pp[2]; { const char* d_ = P_oth + (t & 1) * (4 * PB_P); pp[0] = *(const bf16x8*)(d_); pp[1] = *(const bf16x8*)(d_ + 1024); }
;     const bf16x8 pc[2] = {po[0], po[1]};
;     const bool more = t + 1 < NT;
;     if (more) EQK((t + 1) & 1);
;     const int vb = vlane + (t & 1) * (int)D16_V, vbo = vb + ch * 1024, vbp = vb + (1 - ch) * 1024;
;     SBAR(); pv16d<0>(o, vbo, vbp, pc, pp); SBAR();
	v_pk_add_f32 v[60:61], v[60:61], v[62:63]
	s_mov_b32 s55, 1
	v_pk_add_f32 v[174:175], v[60:61], 0 op_sel_hi:[1,0]
	s_add_u32 s74, s72, 0xc0000
	s_addc_u32 s75, s73, 0
	s_add_u32 s76, s74, 0x60000
	s_addc_u32 s77, s75, 0
	v_lshl_add_u64 v[176:177], s[6:7], 1, v[172:173]
	s_mov_b64 s[6:7], 0
	s_movk_i32 s56, 0x4000
	v_mov_b32_e32 v113, v112
	v_mov_b32_e32 v114, v112
	v_mov_b32_e32 v115, v112
	v_mov_b32_e32 v120, v112
	v_mov_b32_e32 v121, v112
	v_mov_b32_e32 v122, v112
	v_mov_b32_e32 v123, v112
	v_mov_b32_e32 v124, v112
	v_mov_b32_e32 v125, v112
	v_mov_b32_e32 v126, v112
	v_mov_b32_e32 v127, v112
	v_mov_b32_e32 v128, v112
	v_mov_b32_e32 v129, v112
	v_mov_b32_e32 v130, v112
	v_mov_b32_e32 v131, v112
	v_mov_b32_e32 v108, v112
	v_mov_b32_e32 v109, v112
	v_mov_b32_e32 v110, v112
	v_mov_b32_e32 v111, v112
	v_mov_b32_e32 v116, v112
	v_mov_b32_e32 v117, v112
	v_mov_b32_e32 v118, v112
	v_mov_b32_e32 v119, v112
	v_mov_b32_e32 v100, v112
	v_mov_b32_e32 v101, v112
	v_mov_b32_e32 v102, v112
	v_mov_b32_e32 v103, v112
	v_mov_b32_e32 v104, v112
	v_mov_b32_e32 v105, v112
	v_mov_b32_e32 v106, v112
	v_mov_b32_e32 v107, v112
	v_mov_b32_e32 v84, v112
	v_mov_b32_e32 v85, v112
	v_mov_b32_e32 v86, v112
	v_mov_b32_e32 v87, v112
	v_mov_b32_e32 v92, v112
	v_mov_b32_e32 v93, v112
	v_mov_b32_e32 v94, v112
	v_mov_b32_e32 v95, v112
	v_mov_b32_e32 v88, v112
	v_mov_b32_e32 v89, v112
	v_mov_b32_e32 v90, v112
	v_mov_b32_e32 v91, v112
	v_mov_b32_e32 v96, v112
	v_mov_b32_e32 v97, v112
	v_mov_b32_e32 v98, v112
	v_mov_b32_e32 v99, v112
	v_mov_b32_e32 v60, v112
	v_mov_b32_e32 v61, v112
	v_mov_b32_e32 v62, v112
	v_mov_b32_e32 v63, v112
	v_mov_b32_e32 v80, v112
	v_mov_b32_e32 v81, v112
	v_mov_b32_e32 v82, v112
	v_mov_b32_e32 v83, v112
	v_mov_b32_e32 v72, v112
	v_mov_b32_e32 v73, v112
	v_mov_b32_e32 v74, v112
	v_mov_b32_e32 v75, v112
	v_mov_b32_e32 v76, v112
	v_mov_b32_e32 v77, v112
	v_mov_b32_e32 v78, v112
	v_mov_b32_e32 v79, v112
	s_branch .LBB0_1271
.LBB0_1271:
	s_add_i32 s60, s55, -1
	s_and_b32 s57, s60, 1
	s_bitcmp1_b32 s55, 0
	s_cselect_b64 s[22:23], -1, 0
	s_and_b64 s[58:59], s[22:23], exec
	s_cselect_b32 s58, 0x4400, 0
	s_cselect_b32 s85, 0x8200, 0
	s_add_i32 s85, s85, s84
	v_add_u32_e32 v178, s58, v193
	s_waitcnt vmcnt(2) lgkmcnt(0)
	s_barrier
	ds_read_b128 v[132:135], v178
	ds_read_b128 v[136:139], v178 offset:64
	ds_read_b128 v[144:147], v178 offset:4352
	ds_read_b128 v[148:151], v178 offset:4416
	s_mov_b32 m0, s85
	s_nop 0
	global_load_lds_dwordx4 v253, s[74:75]
	s_add_i32 m0, s85, 0x800
	s_nop 0
	global_load_lds_dwordx4 v253, s[74:75] offset:32
	s_add_i32 m0, s85, 0x400
	s_nop 0
	global_load_lds_dwordx4 v253, s[76:77]
	s_add_i32 m0, s85, 0xc00
	s_nop 0
	global_load_lds_dwordx4 v253, s[76:77] offset:32
	s_add_u32 s74, s74, 0xc0000
	s_addc_u32 s75, s75, 0
	s_add_u32 s76, s76, 0xc0000
	s_addc_u32 s77, s77, 0
	s_waitcnt lgkmcnt(3)
	v_mfma_f32_16x16x32_bf16 v[140:143], v[132:135], v[4:7], v[248:251]
	s_mul_i32 s58, s57, 0x8200
	v_mfma_f32_16x16x32_bf16 v[132:135], v[132:135], v[20:23], v[248:251]
	s_waitcnt lgkmcnt(1)
	v_mfma_f32_16x16x32_bf16 v[152:155], v[144:147], v[4:7], v[248:251]
	v_mfma_f32_16x16x32_bf16 v[144:147], v[144:147], v[20:23], v[248:251]
	v_mfma_f32_16x16x32_bf16 v[140:143], v[136:139], v[8:11], v[140:143]
	v_mfma_f32_16x16x32_bf16 v[132:135], v[136:139], v[24:27], v[132:135]
	s_waitcnt lgkmcnt(0)
	v_mfma_f32_16x16x32_bf16 v[136:139], v[148:151], v[8:11], v[152:155]
	v_mfma_f32_16x16x32_bf16 v[144:147], v[148:151], v[24:27], v[144:147]
	ds_read_b128 v[148:151], v178 offset:128
	s_nop 0
	ds_read_b128 v[152:155], v178 offset:192
	s_waitcnt lgkmcnt(1)
	v_mfma_f32_16x16x32_bf16 v[140:143], v[148:151], v[12:15], v[140:143]
	v_mfma_f32_16x16x32_bf16 v[132:135], v[148:151], v[28:31], v[132:135]
	ds_read_b128 v[148:151], v178 offset:4480
	ds_read_b128 v[180:183], v178 offset:4544
	s_waitcnt lgkmcnt(1)
	v_mfma_f32_16x16x32_bf16 v[136:139], v[148:151], v[12:15], v[136:139]
	v_mfma_f32_16x16x32_bf16 v[204:207], v[148:151], v[28:31], v[144:147]
	v_mfma_f32_16x16x32_bf16 v[144:147], v[152:155], v[16:19], v[140:143]
	v_mfma_f32_16x16x32_bf16 v[140:143], v[152:155], v[32:35], v[132:135]
	s_nop 2
	v_lshl_add_u32 v132, s57, 14, v191
	ds_read_b128 v[148:151], v132
	ds_read_b128 v[152:155], v132 offset:1024
	v_add_u32_e32 v132, s58, v194
	s_waitcnt lgkmcnt(2)
	v_mfma_f32_16x16x32_bf16 v[136:139], v[180:183], v[16:19], v[136:139]
	v_add_u32_e32 v179, v132, v195
	v_add_u32_e32 v178, v132, v196
	v_mfma_f32_16x16x32_bf16 v[132:135], v[180:183], v[32:35], v[204:207]
	ds_read_b64_tr_b16 v[180:181], v179 offset:0
	ds_read_b64_tr_b16 v[182:183], v179 offset:0x200
	ds_read_b64_tr_b16 v[204:205], v178 offset:0
	ds_read_b64_tr_b16 v[206:207], v178 offset:0x200
	ds_read_b64_tr_b16 v[208:209], v179 offset:0x820
	ds_read_b64_tr_b16 v[210:211], v179 offset:0xa20
	ds_read_b64_tr_b16 v[212:213], v178 offset:0x820
	ds_read_b64_tr_b16 v[214:215], v178 offset:0xa20
	ds_read_b64_tr_b16 v[216:217], v179 offset:0x1040
	ds_read_b64_tr_b16 v[218:219], v179 offset:0x1240
	ds_read_b64_tr_b16 v[220:221], v178 offset:0x1040
	ds_read_b64_tr_b16 v[222:223], v178 offset:0x1240
	s_waitcnt lgkmcnt(4)
; #define SBAR() __builtin_amdgcn_sched_barrier(0)
; #define MFMA16(a, b, c) __builtin_amdgcn_mfma_f32_16x16x32_bf16(a, b, c, 0, 0, 0)
; template <int D0> __device__ __forceinline__ void pv16d(f32x4a (&o)[8][2], int vbo, int vbp, const bf16x8 (&po)[2], const bf16x8 (&pp)[2]) {
;     ...
;   asm volatile("s_waitcnt lgkmcnt(4)" ::: "memory"); SBAR();
;   o[D0][0] = MFMA16(PK16(a0, a1), po[0], o[D0][0]); o[D0][1] = MFMA16(PK16(a0, a1), po[1], o[D0][1]);
;   o[D0 + 1][0] = MFMA16(PK16(b0, b1), po[0], o[D0 + 1][0]); o[D0 + 1][1] = MFMA16(PK16(b0, b1), po[1], o[D0 + 1][1]);
;   o[D0][0] = MFMA16(PK16(a2, a3), pp[0], o[D0][0]); o[D0][1] = MFMA16(PK16(a2, a3), pp[1], o[D0][1]);
;   o[D0 + 1][0] = MFMA16(PK16(b2, b3), pp[0], o[D0 + 1][0]); o[D0 + 1][1] = MFMA16(PK16(b2, b3), pp[1], o[D0 + 1][1]);
;   SBAR();
;   const s16x4 d0 = TRO(D0 + 3, 0), d1 = TRO(D0 + 3, 1), d2 = TRP(D0 + 3, 0), d3 = TRP(D0 + 3, 1);
;   asm volatile("s_waitcnt lgkmcnt(4)" ::: "memory"); SBAR();
;   o[D0 + 2][0] = MFMA16(PK16(c0, c1), po[0], o[D0 + 2][0]); o[D0 + 2][1] = MFMA16(PK16(c0, c1), po[1], o[D0 + 2][1]);
;   o[D0 + 2][0] = MFMA16(PK16(c2, c3), pp[0], o[D0 + 2][0]); o[D0 + 2][1] = MFMA16(PK16(c2, c3), pp[1], o[D0 + 2][1]);
;   asm volatile("s_waitcnt lgkmcnt(0)" ::: "memory"); SBAR();
;   o[D0 + 3][0] = MFMA16(PK16(d0, d1), po[0], o[D0 + 3][0]); o[D0 + 3][1] = MFMA16(PK16(d0, d1), po[1], o[D0 + 3][1]);
;   o[D0 + 3][0] = MFMA16(PK16(d2, d3), pp[0], o[D0 + 3][0]); o[D0 + 3][1] = MFMA16(PK16(d2, d3), pp[1], o[D0 + 3][1]);
	s_nop 0
	v_mfma_f32_16x16x32_bf16 v[128:131], v[180:183], v[64:67], v[128:131]
	v_mfma_f32_16x16x32_bf16 v[124:127], v[180:183], v[68:71], v[124:127]
	v_mfma_f32_16x16x32_bf16 v[120:123], v[208:211], v[64:67], v[120:123]
	v_mfma_f32_16x16x32_bf16 v[112:115], v[208:211], v[68:71], v[112:115]
	s_waitcnt lgkmcnt(1)
	v_mfma_f32_16x16x32_bf16 v[128:131], v[204:207], v[148:151], v[128:131]
	s_waitcnt lgkmcnt(0)
	v_mfma_f32_16x16x32_bf16 v[124:127], v[204:207], v[152:155], v[124:127]
	v_mfma_f32_16x16x32_bf16 v[120:123], v[212:215], v[148:151], v[120:123]
	v_mfma_f32_16x16x32_bf16 v[112:115], v[212:215], v[152:155], v[112:115]
	ds_read_b64_tr_b16 v[180:181], v179 offset:0x1860
	ds_read_b64_tr_b16 v[182:183], v179 offset:0x1a60
	ds_read_b64_tr_b16 v[204:205], v178 offset:0x1860
	ds_read_b64_tr_b16 v[206:207], v178 offset:0x1a60
	s_waitcnt lgkmcnt(4)
	v_mfma_f32_16x16x32_bf16 v[108:111], v[216:219], v[64:67], v[108:111]
	s_waitcnt lgkmcnt(0)
	ds_read_b64_tr_b16 v[36:37], v179 offset:0x2080
	ds_read_b64_tr_b16 v[38:39], v179 offset:0x2280
	ds_read_b64_tr_b16 v[40:41], v178 offset:0x2080
	ds_read_b64_tr_b16 v[42:43], v178 offset:0x2280
	ds_read_b64_tr_b16 v[44:45], v179 offset:0x28a0
	ds_read_b64_tr_b16 v[46:47], v179 offset:0x2aa0
	ds_read_b64_tr_b16 v[48:49], v178 offset:0x28a0
	ds_read_b64_tr_b16 v[50:51], v178 offset:0x2aa0
	ds_read_b64_tr_b16 v[232:233], v179 offset:0x30c0
	ds_read_b64_tr_b16 v[234:235], v179 offset:0x32c0
	ds_read_b64_tr_b16 v[236:237], v178 offset:0x30c0
	ds_read_b64_tr_b16 v[238:239], v178 offset:0x32c0
	v_mfma_f32_16x16x32_bf16 v[116:119], v[216:219], v[68:71], v[116:119]
	v_mfma_f32_16x16x32_bf16 v[108:111], v[220:223], v[148:151], v[108:111]
	v_mfma_f32_16x16x32_bf16 v[116:119], v[220:223], v[152:155], v[116:119]
	v_mfma_f32_16x16x32_bf16 v[100:103], v[180:183], v[64:67], v[100:103]
	v_mfma_f32_16x16x32_bf16 v[104:107], v[180:183], v[68:71], v[104:107]
	v_mfma_f32_16x16x32_bf16 v[100:103], v[204:207], v[148:151], v[100:103]
	v_mfma_f32_16x16x32_bf16 v[104:107], v[204:207], v[152:155], v[104:107]
	s_waitcnt vmcnt(4)
	s_cmpk_gt_u32 s60, 0x101
	s_cbranch_scc1 .Lvd_kskip
	s_mulk_i32 s57, 0x4400
	v_add_u32_e32 v244, s57, v198
	s_nop 0
	ds_write_b128 v244, v[52:55]
	ds_write_b128 v244, v[56:59] offset:8704
.Lvd_kskip:
	v_lshl_add_u64 v[240:241], v[176:177], 0, s[6:7]
	v_add_co_u32_e32 v242, vcc, s41, v240
	s_nop 1
	v_addc_co_u32_e32 v243, vcc, 0, v241, vcc
	v_add_co_u32_e32 v240, vcc, s42, v240
	s_nop 1
	v_addc_co_u32_e32 v241, vcc, 0, v241, vcc
	global_load_dwordx4 v[52:55], v[242:243], off offset:1024
	global_load_dwordx4 v[56:59], v[240:241], off offset:1024
	s_waitcnt lgkmcnt(4)
	s_nop 0
	v_mfma_f32_16x16x32_bf16 v[84:87], v[36:39], v[64:67], v[84:87]
	v_mfma_f32_16x16x32_bf16 v[92:95], v[36:39], v[68:71], v[92:95]
	v_mfma_f32_16x16x32_bf16 v[88:91], v[44:47], v[64:67], v[88:91]
	v_mfma_f32_16x16x32_bf16 v[96:99], v[44:47], v[68:71], v[96:99]
	v_mfma_f32_16x16x32_bf16 v[84:87], v[40:43], v[148:151], v[84:87]
	v_mfma_f32_16x16x32_bf16 v[92:95], v[40:43], v[152:155], v[92:95]
	v_mfma_f32_16x16x32_bf16 v[88:91], v[48:51], v[148:151], v[88:91]
	v_mfma_f32_16x16x32_bf16 v[96:99], v[48:51], v[152:155], v[96:99]
	ds_read_b64_tr_b16 v[180:181], v179 offset:0x38e0
	ds_read_b64_tr_b16 v[182:183], v179 offset:0x3ae0
	ds_read_b64_tr_b16 v[204:205], v178 offset:0x38e0
	ds_read_b64_tr_b16 v[206:207], v178 offset:0x3ae0
	s_waitcnt lgkmcnt(4)
	v_mfma_f32_16x16x32_bf16 v[60:63], v[232:235], v[64:67], v[60:63]
	s_waitcnt lgkmcnt(0)
	v_mfma_f32_16x16x32_bf16 v[80:83], v[232:235], v[68:71], v[80:83]
	v_mfma_f32_16x16x32_bf16 v[60:63], v[236:239], v[148:151], v[60:63]
	v_mfma_f32_16x16x32_bf16 v[80:83], v[236:239], v[152:155], v[80:83]
	v_mfma_f32_16x16x32_bf16 v[64:67], v[180:183], v[64:67], v[72:75]
	v_mfma_f32_16x16x32_bf16 v[68:71], v[180:183], v[68:71], v[76:79]
	v_mfma_f32_16x16x32_bf16 v[72:75], v[204:207], v[148:151], v[64:67]
	v_mfma_f32_16x16x32_bf16 v[76:79], v[204:207], v[152:155], v[68:71]
	s_nop 4
	v_exp_f32_e32 v144, v144
	v_exp_f32_e32 v148, v145
	v_exp_f32_e32 v146, v146
	v_exp_f32_e32 v150, v147
	v_exp_f32_e32 v145, v140
	v_exp_f32_e32 v149, v141
	v_exp_f32_e32 v147, v142
	v_exp_f32_e32 v151, v143
	v_exp_f32_e32 v136, v136
	v_exp_f32_e32 v140, v137
	v_exp_f32_e32 v138, v138
	v_exp_f32_e32 v142, v139
	v_exp_f32_e32 v137, v132
	v_exp_f32_e32 v141, v133
	v_exp_f32_e32 v139, v134
	v_exp_f32_e32 v143, v135
	s_and_b32 s22, s56, 0x4000
	v_add_u32_e32 v132, s22, v190
	v_cvt_pk_bf16_f32 v64, v144, v148
	v_cvt_pk_bf16_f32 v65, v146, v150
	v_cvt_pk_bf16_f32 v66, v136, v140
	v_cvt_pk_bf16_f32 v67, v138, v142
	v_cvt_pk_bf16_f32 v68, v145, v149
	v_cvt_pk_bf16_f32 v69, v147, v151
	v_cvt_pk_bf16_f32 v70, v137, v141
	v_cvt_pk_bf16_f32 v71, v139, v143
	ds_write_b128 v132, v[64:67]
	ds_write_b128 v132, v[68:71] offset:1024
	v_pk_add_f32 v[132:133], v[144:145], v[148:149]
	v_pk_add_f32 v[134:135], v[146:147], v[150:151]
	s_add_u32 s6, s6, 0xc0000
	v_pk_add_f32 v[132:133], v[132:133], v[134:135]
	v_pk_add_f32 v[134:135], v[136:137], v[140:141]
	v_pk_add_f32 v[136:137], v[138:139], v[142:143]
	s_addc_u32 s7, s7, 0
	v_pk_add_f32 v[134:135], v[134:135], v[136:137]
	s_add_i32 s55, s55, 1
	v_pk_add_f32 v[132:133], v[132:133], v[134:135]
	s_addk_i32 s56, 0x4000
	s_cmp_eq_u32 s6, 0xc240000
	v_pk_add_f32 v[174:175], v[174:175], v[132:133]
	s_cbranch_scc0 .LBB0_1271
